# NA attention: the unit's 8 bias rows copied once into a per-wave LDS slice; per-tile bias fetched by ds_read2_b32 instead of 4 unaligned global dwordx4 (less vector-memory traffic)
# speedup vs baseline: 1.0011x; 1.0011x over previous
.LBB0_1292:
	s_ashr_i32 s47, s33, 4
	v_bfrev_b32_e32 v0, 0.5
	v_med3_i32 v4, s47, 4, v0
	s_lshl_b32 s1, s33, 5
	v_readfirstlane_b32 s0, v4
	s_add_i32 s48, s0, -4
	s_lshl_b32 s0, s47, 6
	s_and_b32 s46, s1, 32
	s_or_b32 s2, s0, s46
	s_bfe_u32 s9, s33, 0x30001
	s_ashr_i32 s3, s2, 31
	s_lshl_b32 s80, s9, 22
	s_lshl_b64 s[0:1], s[2:3], 11
	s_add_u32 s0, s20, s0
	s_addc_u32 s1, s21, s1
	s_lshl_b32 s34, s9, 7
	s_lshl_b32 s3, s9, 8
	s_add_u32 s0, s0, s3
	s_addc_u32 s1, s1, 0
	s_lshl_b32 s3, s9, 21
	s_add_u32 s49, s22, s80
	v_readlane_b32 s35, v255, 17
	s_addc_u32 s50, s23, 0
	s_or_b32 s9, s9, s35
	s_mul_i32 s36, s9, 0x780
	s_mov_b32 s37, s81
	s_lshl_b32 s8, s48, 1
	s_lshl_b64 s[36:37], s[36:37], 2
	s_add_u32 s35, s30, s36
	s_mov_b32 s9, s81
	s_addc_u32 s36, s31, s37
	v_lshl_add_u64 v[0:1], s[0:1], 0, v[176:177]
	v_lshlrev_b32_e32 v2, 1, v172
	v_mov_b32_e32 v3, v177
	s_lshl_b64 s[0:1], s[8:9], 12
	s_lshl_b64 s[8:9], s[8:9], 13
	v_lshl_add_u64 v[0:1], v[0:1], 0, v[2:3]
	v_or_b32_e32 v2, s46, v173
	s_add_u32 s8, s49, s8
	s_sub_i32 s98, s48, s47
	s_addk_i32 s98, 7
	s_lshl_b32 s98, s98, 9
	s_ashr_i32 s99, s98, 31
	s_add_u32 s98, s35, s98
	s_addc_u32 s99, s36, s99
	global_load_dwordx4 v[232:235], v198, s[98:99]
	global_load_dwordx4 v[236:239], v198, s[98:99] offset:1024
	global_load_dwordx4 v[240:243], v198, s[98:99] offset:2048
	global_load_dwordx4 v[244:247], v198, s[98:99] offset:3072
	global_load_dwordx4 v[108:111], v[0:1], off
	global_load_dwordx4 v[104:107], v[0:1], off offset:32
	global_load_dwordx4 v[100:103], v[0:1], off offset:64
	global_load_dwordx4 v[96:99], v[0:1], off offset:96
	global_load_dwordx4 v[92:95], v[0:1], off offset:128
	global_load_dwordx4 v[88:91], v[0:1], off offset:160
	global_load_dwordx4 v[84:87], v[0:1], off offset:192
	global_load_dwordx4 v[80:83], v[0:1], off offset:224
	v_min_u32_e32 v0, 56, v2
	s_addc_u32 s9, s50, s9
	v_mov_b32_e32 v199, v177
	v_sub_u32_e32 v3, 8, v0
	v_lshl_add_u64 v[0:1], s[8:9], 0, v[198:199]
	v_add_co_u32_e32 v0, vcc, s90, v0
	global_load_dwordx4 v[64:67], v198, s[8:9]
	global_load_dwordx4 v[168:171], v198, s[8:9] offset:1024
	global_load_dwordx4 v[164:167], v198, s[8:9] offset:2048
	global_load_dwordx4 v[160:163], v198, s[8:9] offset:3072
	v_addc_co_u32_e32 v1, vcc, 0, v1, vcc
	global_load_dwordx4 v[156:159], v[0:1], off
	global_load_dwordx4 v[152:155], v[0:1], off offset:1024
	global_load_dwordx4 v[148:151], v[0:1], off offset:2048
	global_load_dwordx4 v[144:147], v[0:1], off offset:3072
	v_cmp_lt_u32_e32 vcc, 7, v2
	v_mov_b32_e32 v1, v177
	v_mov_b32_e32 v207, 0
	v_cndmask_b32_e32 v0, 0, v3, vcc
	v_add_u32_e32 v201, v0, v172
	v_lshlrev_b32_e32 v0, 14, v4
	v_add_u32_e32 v0, 0xffff0000, v0
	v_lshl_add_u64 v[0:1], s[80:81], 0, v[0:1]
	s_mov_b32 s46, 0
	s_sub_i32 s37, s48, s47
	v_sub_u32_e32 v199, v208, v2
	v_lshl_add_u64 v[204:205], v[174:175], 0, v[0:1]
	v_mov_b32_e32 v206, 0xff61b1e6
	s_mov_b64 s[8:9], 0
	s_mov_b32 s47, 0
	v_mov_b32_e32 v0, 0
	v_mov_b32_e32 v1, v207
	v_mov_b32_e32 v2, v207
	v_mov_b32_e32 v3, v207
	v_mov_b32_e32 v4, v207
	v_mov_b32_e32 v5, v207
	v_mov_b32_e32 v6, v207
	v_mov_b32_e32 v7, v207
	s_waitcnt vmcnt(16)
	v_mov_b32_e32 v8, v207
	v_mov_b32_e32 v9, v207
	v_mov_b32_e32 v10, v207
	v_mov_b32_e32 v11, v207
	v_mov_b32_e32 v12, v207
	v_mov_b32_e32 v13, v207
	v_mov_b32_e32 v14, v207
	v_mov_b32_e32 v15, v207
	v_mov_b32_e32 v16, 0
	v_mov_b32_e32 v17, v207
	v_mov_b32_e32 v18, v207
	v_mov_b32_e32 v19, v207
	v_mov_b32_e32 v20, v207
	v_mov_b32_e32 v21, v207
	v_mov_b32_e32 v22, v207
	v_mov_b32_e32 v23, v207
	v_mov_b32_e32 v24, v207
	v_mov_b32_e32 v25, v207
	v_mov_b32_e32 v26, v207
	v_mov_b32_e32 v27, v207
	v_mov_b32_e32 v28, v207
	v_mov_b32_e32 v29, v207
	v_mov_b32_e32 v30, v207
	v_mov_b32_e32 v31, v207
	v_mov_b32_e32 v32, 0
	v_mov_b32_e32 v33, v207
	v_mov_b32_e32 v34, v207
	v_mov_b32_e32 v35, v207
	v_mov_b32_e32 v36, v207
	v_mov_b32_e32 v37, v207
	v_mov_b32_e32 v38, v207
	v_mov_b32_e32 v39, v207
	v_mov_b32_e32 v40, v207
	v_mov_b32_e32 v41, v207
	v_mov_b32_e32 v42, v207
	v_mov_b32_e32 v43, v207
	v_mov_b32_e32 v44, v207
	v_mov_b32_e32 v45, v207
	v_mov_b32_e32 v46, v207
	v_mov_b32_e32 v47, v207
	v_mov_b32_e32 v48, 0
	v_mov_b32_e32 v49, v207
	v_mov_b32_e32 v50, v207
	v_mov_b32_e32 v51, v207
	v_mov_b32_e32 v52, v207
	v_mov_b32_e32 v53, v207
	v_mov_b32_e32 v54, v207
	v_mov_b32_e32 v55, v207
	v_mov_b32_e32 v56, v207
	v_mov_b32_e32 v57, v207
	v_mov_b32_e32 v58, v207
	v_mov_b32_e32 v59, v207
	v_mov_b32_e32 v60, v207
	v_mov_b32_e32 v61, v207
	v_mov_b32_e32 v62, v207
	v_mov_b32_e32 v63, v207
	s_and_b32 s99, s33, 7
	s_lshl_b32 s99, s99, 12
	v_add_u32_e32 v249, s99, v198
	ds_write_b128 v249, v[232:235]
	ds_write_b128 v249, v[236:239] offset:1024
	ds_write_b128 v249, v[240:243] offset:2048
	ds_write_b128 v249, v[244:247] offset:3072
	s_lshr_b32 s98, s47, 1
	s_lshl_b32 s98, s98, 9
	s_add_i32 s98, s98, s99
	s_and_b32 s50, s46, 32
	v_add_lshl_u32 v248, s50, v199, 2
	v_add_u32_e32 v249, s98, v248
	ds_read2_b32 v[232:233], v249 offset1:1
	ds_read2_b32 v[234:235], v249 offset0:2 offset1:3
	ds_read2_b32 v[236:237], v249 offset0:4 offset1:5
	ds_read2_b32 v[238:239], v249 offset0:6 offset1:7
	ds_read2_b32 v[240:241], v249 offset0:16 offset1:17
	ds_read2_b32 v[242:243], v249 offset0:18 offset1:19
	ds_read2_b32 v[244:245], v249 offset0:20 offset1:21
	ds_read2_b32 v[246:247], v249 offset0:22 offset1:23
	s_waitcnt lgkmcnt(0)
.LBB0_1293:
	v_mov_b32_e32 v203, v207
	v_mov_b32_e32 v209, v206
	v_lshl_add_u64 v[206:207], v[204:205], 0, s[8:9]
	s_mov_b32 s48, 0x35000000
	v_add_co_u32_e32 v68, vcc, s48, v206
	s_mov_b32 s48, 0x35001000
	s_nop 0
	v_addc_co_u32_e32 v69, vcc, 0, v207, vcc
	v_add_co_u32_e32 v70, vcc, s48, v206
	s_lshr_b32 s48, s47, 1
	s_add_i32 s48, s48, s37
	s_lshl_b32 s48, s48, 7
	s_ashr_i32 s49, s48, 31
	s_lshl_b64 s[48:49], s[48:49], 2
	s_add_u32 s48, s35, s48
	v_addc_co_u32_e32 v71, vcc, 0, v207, vcc
	s_addc_u32 s49, s36, s49
	s_and_b32 s50, s46, 32
	global_load_dwordx4 v[136:139], v[70:71], off offset:-4096
	global_load_dwordx4 v[140:143], v[68:69], off offset:1024
	global_load_dwordx4 v[128:131], v[68:69], off offset:2048
	global_load_dwordx4 v[132:135], v[68:69], off offset:3072
	global_load_dwordx4 v[120:123], v[70:71], off
	global_load_dwordx4 v[124:127], v[70:71], off offset:1024
	global_load_dwordx4 v[112:115], v[70:71], off offset:2048
	global_load_dwordx4 v[116:119], v[70:71], off offset:3072
	s_waitcnt vmcnt(15)
	v_mfma_f32_32x32x16_bf16 v[64:79], v[64:67], v[108:111], 0
	s_movk_i32 s48, 0xffef
	s_add_i32 s47, s47, 1
	s_add_u32 s8, s8, 0x2000
	s_addc_u32 s9, s9, 0
	s_add_i32 s46, s46, 32
	s_waitcnt vmcnt(14)
	v_mfma_f32_32x32x16_bf16 v[64:79], v[168:171], v[104:107], v[64:79]
	s_waitcnt vmcnt(13)
	v_mfma_f32_32x32x16_bf16 v[64:79], v[164:167], v[100:103], v[64:79]
	s_waitcnt vmcnt(12)
	v_mfma_f32_32x32x16_bf16 v[64:79], v[160:163], v[96:99], v[64:79]
	s_waitcnt vmcnt(11)
	v_mfma_f32_32x32x16_bf16 v[64:79], v[156:159], v[92:95], v[64:79]
	v_add_u32_e32 v156, s50, v201
	v_cmp_gt_u32_e32 vcc, 16, v156
	s_waitcnt vmcnt(10)
	v_mfma_f32_32x32x16_bf16 v[64:79], v[152:155], v[88:91], v[64:79]
	s_waitcnt vmcnt(9)
	v_mfma_f32_32x32x16_bf16 v[64:79], v[148:151], v[84:87], v[64:79]
	s_waitcnt vmcnt(8)
	v_mfma_f32_32x32x16_bf16 v[64:79], v[144:147], v[80:83], v[64:79]
	s_nop 3
	s_nop 7
	v_add_f32_e32 v64, v64, v232
	v_cndmask_b32_e32 v217, v222, v64, vcc
	v_add_u32_e32 v64, 1, v156
	v_cmp_gt_u32_e32 vcc, 16, v64
	v_add_f32_e32 v64, v65, v233
	s_nop 0
	v_cndmask_b32_e32 v216, v222, v64, vcc
	v_add_u32_e32 v64, 2, v156
	v_cmp_gt_u32_e32 vcc, 16, v64
	v_add_f32_e32 v64, v66, v234
	s_nop 0
	v_cndmask_b32_e32 v215, v222, v64, vcc
	v_add_u32_e32 v64, 3, v156
	v_cmp_gt_u32_e32 vcc, 16, v64
	v_add_f32_e32 v64, v67, v235
	s_nop 0
	v_cndmask_b32_e32 v214, v222, v64, vcc
	v_add_u32_e32 v64, 4, v156
	v_cmp_gt_u32_e32 vcc, 16, v64
	v_add_f32_e32 v64, v68, v236
	s_nop 0
	v_cndmask_b32_e32 v213, v222, v64, vcc
	v_add_u32_e32 v64, 5, v156
	v_cmp_gt_u32_e32 vcc, 16, v64
	v_add_f32_e32 v64, v69, v237
	s_nop 0
	v_cndmask_b32_e32 v212, v222, v64, vcc
	v_add_u32_e32 v64, 6, v156
	v_cmp_gt_u32_e32 vcc, 16, v64
	v_add_f32_e32 v64, v70, v238
	s_nop 0
	v_cndmask_b32_e32 v211, v222, v64, vcc
	v_add_u32_e32 v64, 7, v156
	v_cmp_gt_u32_e32 vcc, 16, v64
	v_add_f32_e32 v64, v71, v239
	s_nop 0
	v_cndmask_b32_e32 v210, v222, v64, vcc
	v_cmp_lt_u32_e32 vcc, s48, v156
	v_add_f32_e32 v64, v72, v240
	s_mov_b32 s48, 0x33002000
	v_cndmask_b32_e32 v221, v222, v64, vcc
	v_add_u32_e32 v64, 17, v156
	v_cmp_gt_u32_e32 vcc, 16, v64
	v_add_f32_e32 v64, v73, v241
	s_nop 0
	v_cndmask_b32_e32 v220, v222, v64, vcc
	v_add_u32_e32 v64, 18, v156
	v_cmp_gt_u32_e32 vcc, 16, v64
	v_add_f32_e32 v64, v74, v242
	s_nop 0
	v_cndmask_b32_e32 v219, v222, v64, vcc
	v_add_u32_e32 v64, 19, v156
	v_cmp_gt_u32_e32 vcc, 16, v64
	v_add_f32_e32 v64, v75, v243
	s_nop 0
	v_cndmask_b32_e32 v218, v222, v64, vcc
	v_add_u32_e32 v64, 20, v156
	v_cmp_gt_u32_e32 vcc, 16, v64
	v_add_f32_e32 v64, v76, v244
	s_nop 0
	v_cndmask_b32_e32 v75, v222, v64, vcc
	v_add_u32_e32 v64, 21, v156
	v_cmp_gt_u32_e32 vcc, 16, v64
	v_add_f32_e32 v64, v77, v245
	s_nop 0
	v_cndmask_b32_e32 v74, v222, v64, vcc
	v_add_u32_e32 v64, 22, v156
	v_cmp_gt_u32_e32 vcc, 16, v64
	v_add_f32_e32 v64, v78, v246
	s_nop 0
	v_cndmask_b32_e32 v73, v222, v64, vcc
	v_add_u32_e32 v64, 23, v156
	v_cmp_gt_u32_e32 vcc, 16, v64
	v_add_f32_e32 v64, v79, v247
	s_nop 0
	v_cndmask_b32_e32 v72, v222, v64, vcc
	s_lshr_b32 s98, s47, 1
	s_lshl_b32 s98, s98, 9
	s_add_i32 s98, s98, s99
	s_and_b32 s50, s46, 32
	v_add_lshl_u32 v248, s50, v199, 2
	v_add_u32_e32 v249, s98, v248
	ds_read2_b32 v[232:233], v249 offset1:1
	ds_read2_b32 v[234:235], v249 offset0:2 offset1:3
	ds_read2_b32 v[236:237], v249 offset0:4 offset1:5
	ds_read2_b32 v[238:239], v249 offset0:6 offset1:7
	ds_read2_b32 v[240:241], v249 offset0:16 offset1:17
	ds_read2_b32 v[242:243], v249 offset0:18 offset1:19
	ds_read2_b32 v[244:245], v249 offset0:20 offset1:21
	ds_read2_b32 v[246:247], v249 offset0:22 offset1:23
	s_cmp_lg_u32 s8, 0x1e000
	v_add_co_u32_e32 v68, vcc, s48, v206
	s_mov_b32 s48, 0x33003000
	s_nop 0
	v_addc_co_u32_e32 v69, vcc, 0, v207, vcc
	v_add_co_u32_e32 v70, vcc, s48, v206
	s_nop 1
	v_addc_co_u32_e32 v71, vcc, 0, v207, vcc
	global_load_dwordx4 v[64:67], v[70:71], off offset:-4096
	global_load_dwordx4 v[168:171], v[68:69], off offset:1024
	global_load_dwordx4 v[164:167], v[68:69], off offset:2048
	global_load_dwordx4 v[160:163], v[68:69], off offset:3072
	global_load_dwordx4 v[156:159], v[70:71], off
	global_load_dwordx4 v[152:155], v[70:71], off offset:1024
	global_load_dwordx4 v[148:151], v[70:71], off offset:2048
	global_load_dwordx4 v[144:147], v[70:71], off offset:3072
	v_max3_f32 v68, v217, s11, v216
	v_max3_f32 v68, v68, v215, v214
	v_max3_f32 v68, v68, v213, v212
	v_max3_f32 v68, v68, v211, v210
	v_max3_f32 v68, v68, v221, v220
	v_max3_f32 v68, v68, v219, v218
	v_mbcnt_lo_u32_b32 v69, -1, 0
	v_mbcnt_hi_u32_b32 v69, -1, v69
	v_max3_f32 v68, v68, v75, v74
	v_lshlrev_b32_e32 v69, 2, v69
	v_max3_f32 v68, v68, v73, v72
	v_xor_b32_e32 v69, 0x80, v69
	ds_bpermute_b32 v69, v69, v68
	s_waitcnt lgkmcnt(0)
	v_max3_f32 v206, v209, v68, v69
	v_sub_f32_e32 v69, v217, v206
	v_exp_f32_e32 v69, v69
	v_sub_f32_e32 v70, v216, v206
	v_exp_f32_e32 v70, v70
	v_sub_f32_e32 v71, v215, v206
	v_exp_f32_e32 v71, v71
	v_sub_f32_e32 v76, v214, v206
	v_exp_f32_e32 v76, v76
	v_sub_f32_e32 v77, v213, v206
	v_sub_f32_e32 v72, v72, v206
	v_exp_f32_e32 v77, v77
	v_sub_f32_e32 v78, v212, v206
	v_exp_f32_e32 v184, v72
	v_add_f32_e32 v72, 0, v69
	v_exp_f32_e32 v78, v78
	v_sub_f32_e32 v79, v211, v206
	v_add_f32_e32 v72, v70, v72
	v_exp_f32_e32 v79, v79
	v_sub_f32_e32 v178, v210, v206
	v_add_f32_e32 v72, v71, v72
	v_exp_f32_e32 v178, v178
	v_sub_f32_e32 v179, v221, v206
	v_add_f32_e32 v72, v76, v72
	v_exp_f32_e32 v179, v179
	v_sub_f32_e32 v180, v220, v206
	v_add_f32_e32 v72, v77, v72
	v_exp_f32_e32 v180, v180
	v_sub_f32_e32 v181, v219, v206
	v_add_f32_e32 v72, v78, v72
	v_exp_f32_e32 v181, v181
	v_sub_f32_e32 v182, v218, v206
	v_add_f32_e32 v72, v79, v72
	v_exp_f32_e32 v182, v182
	v_sub_f32_e32 v75, v75, v206
	v_add_f32_e32 v72, v178, v72
	v_exp_f32_e32 v75, v75
	v_sub_f32_e32 v74, v74, v206
	v_add_f32_e32 v72, v179, v72
	v_exp_f32_e32 v74, v74
	v_sub_f32_e32 v73, v73, v206
	v_add_f32_e32 v72, v180, v72
	v_exp_f32_e32 v183, v73
	v_add_f32_e32 v72, v181, v72
	v_add_f32_e32 v72, v182, v72
	v_sub_f32_e32 v68, v209, v206
	v_add_f32_e32 v72, v75, v72
	v_exp_f32_e32 v68, v68
	v_add_f32_e32 v72, v74, v72
	v_add_f32_e32 v72, v183, v72
	v_add_f32_e32 v207, v184, v72
	v_bfe_u32 v72, v178, 16, 1
	v_bfe_u32 v73, v78, 16, 1
	v_bfe_u32 v185, v76, 16, 1
	v_bfe_u32 v186, v70, 16, 1
	v_add3_u32 v70, v70, v186, s25
	v_add3_u32 v76, v76, v185, s25
	v_add3_u32 v78, v78, v73, s25
	v_add3_u32 v72, v178, v72, s25
	v_bfe_u32 v73, v69, 16, 1
	v_bfe_u32 v178, v71, 16, 1
	v_bfe_u32 v185, v77, 16, 1
	v_bfe_u32 v186, v79, 16, 1
	v_pk_mul_f32 v[62:63], v[62:63], v[68:69] op_sel_hi:[1,0]
	v_pk_mul_f32 v[60:61], v[60:61], v[68:69] op_sel_hi:[1,0]
	v_pk_mul_f32 v[58:59], v[58:59], v[68:69] op_sel_hi:[1,0]
	v_pk_mul_f32 v[56:57], v[56:57], v[68:69] op_sel_hi:[1,0]
	v_pk_mul_f32 v[54:55], v[54:55], v[68:69] op_sel_hi:[1,0]
	v_pk_mul_f32 v[52:53], v[52:53], v[68:69] op_sel_hi:[1,0]
	v_pk_mul_f32 v[50:51], v[50:51], v[68:69] op_sel_hi:[1,0]
	v_pk_mul_f32 v[48:49], v[48:49], v[68:69] op_sel_hi:[1,0]
	v_pk_mul_f32 v[46:47], v[46:47], v[68:69] op_sel_hi:[1,0]
	v_pk_mul_f32 v[44:45], v[44:45], v[68:69] op_sel_hi:[1,0]
	v_pk_mul_f32 v[42:43], v[42:43], v[68:69] op_sel_hi:[1,0]
	v_pk_mul_f32 v[40:41], v[40:41], v[68:69] op_sel_hi:[1,0]
	v_pk_mul_f32 v[38:39], v[38:39], v[68:69] op_sel_hi:[1,0]
	v_pk_mul_f32 v[36:37], v[36:37], v[68:69] op_sel_hi:[1,0]
	v_pk_mul_f32 v[34:35], v[34:35], v[68:69] op_sel_hi:[1,0]
	v_pk_mul_f32 v[32:33], v[32:33], v[68:69] op_sel_hi:[1,0]
	v_pk_mul_f32 v[30:31], v[30:31], v[68:69] op_sel_hi:[1,0]
	v_pk_mul_f32 v[28:29], v[28:29], v[68:69] op_sel_hi:[1,0]
	v_pk_mul_f32 v[26:27], v[26:27], v[68:69] op_sel_hi:[1,0]
	v_pk_mul_f32 v[24:25], v[24:25], v[68:69] op_sel_hi:[1,0]
	v_pk_mul_f32 v[22:23], v[22:23], v[68:69] op_sel_hi:[1,0]
	v_pk_mul_f32 v[20:21], v[20:21], v[68:69] op_sel_hi:[1,0]
	v_pk_mul_f32 v[18:19], v[18:19], v[68:69] op_sel_hi:[1,0]
	v_pk_mul_f32 v[16:17], v[16:17], v[68:69] op_sel_hi:[1,0]
	v_pk_mul_f32 v[14:15], v[14:15], v[68:69] op_sel_hi:[1,0]
	v_pk_mul_f32 v[12:13], v[12:13], v[68:69] op_sel_hi:[1,0]
	v_pk_mul_f32 v[10:11], v[10:11], v[68:69] op_sel_hi:[1,0]
	v_pk_mul_f32 v[8:9], v[8:9], v[68:69] op_sel_hi:[1,0]
	v_pk_mul_f32 v[6:7], v[6:7], v[68:69] op_sel_hi:[1,0]
	v_pk_mul_f32 v[4:5], v[4:5], v[68:69] op_sel_hi:[1,0]
	v_pk_mul_f32 v[2:3], v[2:3], v[68:69] op_sel_hi:[1,0]
	v_pk_mul_f32 v[0:1], v[0:1], v[68:69] op_sel_hi:[1,0]
	v_add3_u32 v79, v79, v186, s25
	v_add3_u32 v77, v77, v185, s25
	v_add3_u32 v71, v71, v178, s25
	v_add3_u32 v69, v69, v73, s25
	v_lshrrev_b32_e32 v69, 16, v69
	v_lshrrev_b32_e32 v71, 16, v71
	v_lshrrev_b32_e32 v77, 16, v77
	v_lshrrev_b32_e32 v73, 16, v79
	v_and_or_b32 v73, v72, s10, v73
	v_and_or_b32 v72, v78, s10, v77
	v_and_or_b32 v71, v76, s10, v71
	v_and_or_b32 v70, v70, s10, v69
	v_bfe_u32 v76, v74, 16, 1
	v_bfe_u32 v77, v182, 16, 1
	s_waitcnt vmcnt(8)
	v_mfma_f32_32x32x16_bf16 v[48:63], v[136:139], v[70:73], v[48:63]
	v_bfe_u32 v78, v180, 16, 1
	v_add3_u32 v78, v180, v78, s25
	v_add3_u32 v79, v182, v77, s25
	v_add3_u32 v74, v74, v76, s25
	v_bfe_u32 v76, v179, 16, 1
	v_bfe_u32 v77, v181, 16, 1
	v_bfe_u32 v178, v75, 16, 1
	v_mfma_f32_32x32x16_bf16 v[32:47], v[128:131], v[70:73], v[32:47]
	v_bfe_u32 v180, v183, 16, 1
	v_bfe_u32 v69, v184, 16, 1
	v_add3_u32 v180, v183, v180, s25
	v_add3_u32 v75, v75, v178, s25
	v_add3_u32 v77, v181, v77, s25
	v_add3_u32 v76, v179, v76, s25
	v_add3_u32 v69, v184, v69, s25
	v_mfma_f32_32x32x16_bf16 v[16:31], v[120:123], v[70:73], v[16:31]
	v_lshrrev_b32_e32 v178, 16, v76
	v_lshrrev_b32_e32 v179, 16, v77
	v_lshrrev_b32_e32 v75, 16, v75
	v_lshrrev_b32_e32 v76, 16, v180
	v_and_or_b32 v77, v69, s10, v76
	v_and_or_b32 v76, v74, s10, v75
	v_and_or_b32 v75, v79, s10, v179
	v_mfma_f32_32x32x16_bf16 v[0:15], v[112:115], v[70:73], v[0:15]
	v_and_or_b32 v74, v78, s10, v178
	v_fmac_f32_e32 v207, v203, v68
	s_nop 0
	v_mfma_f32_32x32x16_bf16 v[48:63], v[140:143], v[74:77], v[48:63]
	v_mfma_f32_32x32x16_bf16 v[32:47], v[132:135], v[74:77], v[32:47]
	v_mfma_f32_32x32x16_bf16 v[16:31], v[124:127], v[74:77], v[16:31]
	v_mfma_f32_32x32x16_bf16 v[0:15], v[116:119], v[74:77], v[0:15]
	s_cbranch_scc1 .LBB0_1293
	s_waitcnt vmcnt(7)
	v_mfma_f32_32x32x16_bf16 v[64:79], v[64:67], v[108:111], 0
	s_lshl_b32 s3, s3, 1
	s_add_u32 s3, s28, s3
	s_addc_u32 s8, s29, 0
	s_mul_hi_i32 s9, s2, 0x1400
	s_mulk_i32 s2, 0x1400
	s_add_u32 s46, s18, s2
	s_addc_u32 s9, s19, s9
	s_lshl_b64 s[0:1], s[0:1], 1
	s_add_u32 s2, s3, s0
	s_waitcnt vmcnt(6)
	v_mfma_f32_32x32x16_bf16 v[64:79], v[168:171], v[104:107], v[64:79]
	s_addc_u32 s3, s8, s1
	s_lshl_b32 s0, s34, 1
	s_add_u32 s0, s46, s0
	s_addc_u32 s1, s9, 0
	s_lshl_b32 s8, s37, 7
	s_addk_i32 s8, 0x700
	s_ashr_i32 s9, s8, 31
	s_lshl_b64 s[8:9], s[8:9], 2
	s_add_u32 s8, s35, s8
	s_addc_u32 s9, s36, s9
	s_waitcnt vmcnt(5)
	v_mfma_f32_32x32x16_bf16 v[64:79], v[164:167], v[100:103], v[64:79]
	v_lshlrev_b32_e32 v100, 2, v199
	global_load_dwordx4 v[120:123], v100, s[8:9] offset:144
	global_load_dwordx4 v[124:127], v100, s[8:9] offset:128
	global_load_dwordx4 v[116:119], v100, s[8:9] offset:208
	global_load_dwordx4 v[128:131], v100, s[8:9] offset:192
	v_mov_b32_e32 v199, v177
	v_add_u32_e32 v132, 32, v201
	v_add_u32_e32 v133, 33, v201
	v_add_u32_e32 v134, 34, v201
	s_waitcnt vmcnt(8)
	v_mfma_f32_32x32x16_bf16 v[64:79], v[160:163], v[96:99], v[64:79]
	v_add_u32_e32 v135, 35, v201
	v_add_u32_e32 v136, 36, v201
	v_add_u32_e32 v137, 37, v201
	v_add_u32_e32 v138, 38, v201
	v_add_u32_e32 v139, 39, v201
	v_mov_b32_e32 v203, v177
	s_add_i32 s33, s33, s5
	s_waitcnt vmcnt(7)
	v_mfma_f32_32x32x16_bf16 v[64:79], v[156:159], v[92:95], v[64:79]
	v_lshl_add_u64 v[92:93], s[2:3], 0, v[198:199]
	s_mov_b32 s2, 0x1f000
	v_add_co_u32_e32 v100, vcc, s2, v92
	s_mov_b32 s2, 0x1e000
	s_nop 0
	v_addc_co_u32_e32 v101, vcc, 0, v93, vcc
	s_waitcnt vmcnt(6)
	v_mfma_f32_32x32x16_bf16 v[64:79], v[152:155], v[88:91], v[64:79]
	v_add_co_u32_e32 v102, vcc, s2, v92
	s_cmpk_gt_i32 s33, 0xfff
	s_nop 0
	v_addc_co_u32_e32 v103, vcc, 0, v93, vcc
	v_cmp_gt_u32_e32 vcc, 16, v132
	s_waitcnt vmcnt(5)
	v_mfma_f32_32x32x16_bf16 v[64:79], v[148:151], v[84:87], v[64:79]
	global_load_dwordx4 v[108:111], v[102:103], off offset:1024
	global_load_dwordx4 v[104:107], v[102:103], off offset:2048
	global_load_dwordx4 v[96:99], v[100:101], off
	global_load_dwordx4 v[92:95], v[100:101], off offset:1024
	global_load_dwordx4 v[88:91], v[100:101], off offset:2048
	global_load_dwordx4 v[84:87], v[100:101], off offset:3072
	global_load_dwordx4 v[112:115], v[100:101], off offset:-4096
	s_nop 0
	global_load_dwordx4 v[100:103], v[102:103], off offset:3072
	s_waitcnt vmcnt(12)
	v_mfma_f32_32x32x16_bf16 v[64:79], v[144:147], v[80:83], v[64:79]
	s_waitcnt vmcnt(11)
	v_mov_b32_e32 v80, v122
	s_waitcnt vmcnt(10)
	v_mov_b32_e32 v81, v127
	v_mov_b32_e32 v82, v121
	v_mov_b32_e32 v83, v124
	v_mov_b32_e32 v121, v123
	v_mov_b32_e32 v122, v126
	s_waitcnt vmcnt(8)
	v_mov_b32_e32 v123, v129
	s_nop 1
	v_add_f32_e32 v64, v64, v83
	v_add_f32_e32 v65, v65, v125
	v_cndmask_b32_e32 v64, v222, v64, vcc
	v_cmp_gt_u32_e32 vcc, 16, v133
	v_add_f32_e32 v66, v66, v122
	v_add_f32_e32 v67, v67, v81
	v_cndmask_b32_e32 v65, v222, v65, vcc
	v_cmp_gt_u32_e32 vcc, 16, v134
	v_add_f32_e32 v68, v68, v120
	v_add_f32_e32 v69, v69, v82
	v_cndmask_b32_e32 v66, v222, v66, vcc
	v_cmp_gt_u32_e32 vcc, 16, v135
	v_add_f32_e32 v70, v70, v80
	v_mov_b32_e32 v124, v131
	v_cndmask_b32_e32 v67, v222, v67, vcc
	v_cmp_gt_u32_e32 vcc, 16, v136
	v_mov_b32_e32 v126, v128
	v_add_f32_e32 v71, v71, v121
	v_cndmask_b32_e32 v68, v222, v68, vcc
	v_cmp_gt_u32_e32 vcc, 16, v137
	v_add_u32_e32 v80, 49, v201
	v_add_f32_e32 v72, v72, v126
	v_cndmask_b32_e32 v69, v222, v69, vcc
	v_cmp_gt_u32_e32 vcc, 16, v138
	v_add_f32_e32 v73, v73, v123
	v_add_f32_e32 v74, v74, v130
	v_cndmask_b32_e32 v70, v222, v70, vcc
	v_cmp_gt_u32_e32 vcc, 16, v139
	v_add_f32_e32 v75, v75, v124
	v_add_f32_e32 v76, v76, v116
	v_cndmask_b32_e32 v71, v222, v71, vcc
	v_cmp_lt_u32_e32 vcc, 48, v132
	v_add_f32_e32 v77, v77, v117
	v_add_f32_e32 v78, v78, v118
	v_cndmask_b32_e32 v72, v222, v72, vcc
	v_cmp_gt_u32_e32 vcc, 16, v80
	v_add_u32_e32 v80, 50, v201
	v_add_f32_e32 v79, v79, v119
	v_cndmask_b32_e32 v73, v222, v73, vcc
	v_cmp_gt_u32_e32 vcc, 16, v80
	v_add_u32_e32 v80, 51, v201
	v_mbcnt_lo_u32_b32 v81, -1, 0
	v_mbcnt_hi_u32_b32 v81, -1, v81
	s_nop 0
	v_cndmask_b32_e32 v74, v222, v74, vcc
	v_cmp_gt_u32_e32 vcc, 16, v80
	v_add_u32_e32 v80, 52, v201
	v_lshlrev_b32_e32 v81, 2, v81
	v_cndmask_b32_e32 v75, v222, v75, vcc
	v_cmp_gt_u32_e32 vcc, 16, v80
	v_add_u32_e32 v80, 53, v201
	v_xor_b32_e32 v81, 0x80, v81
	v_cndmask_b32_e32 v76, v222, v76, vcc
	v_cmp_gt_u32_e32 vcc, 16, v80
	v_add_u32_e32 v80, 54, v201
	s_nop 0
	v_cndmask_b32_e32 v77, v222, v77, vcc
	v_cmp_gt_u32_e32 vcc, 16, v80
	v_add_u32_e32 v80, 55, v201
	v_mov_b32_e32 v201, v177
	v_cndmask_b32_e32 v78, v222, v78, vcc
	v_cmp_gt_u32_e32 vcc, 16, v80
	v_max3_f32 v80, v64, s11, v65
	v_max3_f32 v80, v80, v66, v67
	v_max3_f32 v80, v80, v68, v69
	v_max3_f32 v80, v80, v70, v71
	v_max3_f32 v80, v80, v72, v73
	v_max3_f32 v80, v80, v74, v75
	v_cndmask_b32_e32 v79, v222, v79, vcc
	v_max3_f32 v80, v80, v76, v77
	v_max3_f32 v80, v80, v78, v79
	ds_bpermute_b32 v81, v81, v80
	s_waitcnt lgkmcnt(0)
	v_max3_f32 v80, v206, v80, v81
	v_sub_f32_e32 v64, v64, v80
	v_exp_f32_e32 v82, v64
	v_sub_f32_e32 v64, v65, v80
	v_exp_f32_e32 v65, v64
	v_sub_f32_e32 v64, v66, v80
	v_exp_f32_e32 v83, v64
	v_sub_f32_e32 v64, v67, v80
	v_exp_f32_e32 v116, v64
	v_sub_f32_e32 v64, v68, v80
	v_exp_f32_e32 v117, v64
	v_sub_f32_e32 v64, v69, v80
	v_exp_f32_e32 v118, v64
	v_sub_f32_e32 v64, v70, v80
	v_exp_f32_e32 v119, v64
	v_sub_f32_e32 v64, v71, v80
	v_exp_f32_e32 v120, v64
	v_sub_f32_e32 v64, v72, v80
	v_exp_f32_e32 v121, v64
	v_sub_f32_e32 v64, v73, v80
	v_exp_f32_e32 v122, v64
	v_sub_f32_e32 v64, v74, v80
	v_exp_f32_e32 v74, v64
	v_sub_f32_e32 v64, v75, v80
	v_exp_f32_e32 v75, v64
	v_sub_f32_e32 v64, v76, v80
	v_sub_f32_e32 v66, v78, v80
	v_sub_f32_e32 v81, v206, v80
	v_exp_f32_e32 v76, v64
	v_sub_f32_e32 v64, v77, v80
	v_exp_f32_e32 v78, v66
	v_sub_f32_e32 v66, v79, v80
	v_bfe_u32 v68, v116, 16, 1
	v_bfe_u32 v69, v65, 16, 1
	v_exp_f32_e32 v77, v64
	v_exp_f32_e32 v64, v81
	v_exp_f32_e32 v79, v66
	v_add3_u32 v70, v65, v69, s25
	v_add3_u32 v71, v116, v68, s25
	v_bfe_u32 v68, v82, 16, 1
	v_bfe_u32 v69, v83, 16, 1
	v_bfe_u32 v72, v117, 16, 1
	v_bfe_u32 v73, v119, 16, 1
	v_bfe_u32 v66, v120, 16, 1
	v_bfe_u32 v67, v118, 16, 1
	v_add3_u32 v73, v119, v73, s25
	v_add3_u32 v72, v117, v72, s25
	v_add3_u32 v69, v83, v69, s25
	v_add3_u32 v68, v82, v68, s25
	v_add3_u32 v67, v118, v67, s25
	v_add3_u32 v66, v120, v66, s25
	v_lshrrev_b32_e32 v80, 16, v68
	v_lshrrev_b32_e32 v81, 16, v69
	v_lshrrev_b32_e32 v68, 16, v72
	v_lshrrev_b32_e32 v69, 16, v73
	v_bfe_u32 v72, v75, 16, 1
	v_bfe_u32 v73, v122, 16, 1
	v_and_or_b32 v69, v66, s10, v69
	v_and_or_b32 v68, v67, s10, v68
	v_and_or_b32 v67, v71, s10, v81
	v_and_or_b32 v66, v70, s10, v80
	v_add3_u32 v80, v122, v73, s25
	v_add3_u32 v81, v75, v72, s25
	v_bfe_u32 v72, v121, 16, 1
	v_bfe_u32 v73, v74, 16, 1
	v_bfe_u32 v124, v78, 16, 1
	v_pk_mul_f32 v[62:63], v[62:63], v[64:65] op_sel_hi:[1,0]
	v_pk_mul_f32 v[60:61], v[60:61], v[64:65] op_sel_hi:[1,0]
	v_pk_mul_f32 v[58:59], v[58:59], v[64:65] op_sel_hi:[1,0]
	v_pk_mul_f32 v[56:57], v[56:57], v[64:65] op_sel_hi:[1,0]
	v_pk_mul_f32 v[54:55], v[54:55], v[64:65] op_sel_hi:[1,0]
	v_pk_mul_f32 v[52:53], v[52:53], v[64:65] op_sel_hi:[1,0]
	v_pk_mul_f32 v[50:51], v[50:51], v[64:65] op_sel_hi:[1,0]
	v_pk_mul_f32 v[48:49], v[48:49], v[64:65] op_sel_hi:[1,0]
	v_bfe_u32 v70, v79, 16, 1
	v_add3_u32 v124, v78, v124, s25
	v_add3_u32 v73, v74, v73, s25
	v_add3_u32 v72, v121, v72, s25
	v_add3_u32 v70, v79, v70, s25
	v_lshrrev_b32_e32 v125, 16, v72
	s_waitcnt vmcnt(1)
	v_mfma_f32_32x32x16_bf16 v[48:63], v[112:115], v[66:69], v[48:63]
	v_lshrrev_b32_e32 v112, 16, v73
	v_lshrrev_b32_e32 v73, 16, v124
	v_and_or_b32 v73, v70, s10, v73
	v_and_or_b32 v70, v80, s10, v125
	v_add_f32_e32 v80, 0, v82
	v_pk_mul_f32 v[46:47], v[46:47], v[64:65] op_sel_hi:[1,0]
	v_pk_mul_f32 v[44:45], v[44:45], v[64:65] op_sel_hi:[1,0]
	v_pk_mul_f32 v[42:43], v[42:43], v[64:65] op_sel_hi:[1,0]
	v_pk_mul_f32 v[40:41], v[40:41], v[64:65] op_sel_hi:[1,0]
	v_pk_mul_f32 v[38:39], v[38:39], v[64:65] op_sel_hi:[1,0]
	v_pk_mul_f32 v[36:37], v[36:37], v[64:65] op_sel_hi:[1,0]
	v_pk_mul_f32 v[34:35], v[34:35], v[64:65] op_sel_hi:[1,0]
	v_pk_mul_f32 v[32:33], v[32:33], v[64:65] op_sel_hi:[1,0]
	v_pk_mul_f32 v[30:31], v[30:31], v[64:65] op_sel_hi:[1,0]
	v_pk_mul_f32 v[28:29], v[28:29], v[64:65] op_sel_hi:[1,0]
	v_pk_mul_f32 v[26:27], v[26:27], v[64:65] op_sel_hi:[1,0]
	v_pk_mul_f32 v[24:25], v[24:25], v[64:65] op_sel_hi:[1,0]
	v_pk_mul_f32 v[22:23], v[22:23], v[64:65] op_sel_hi:[1,0]
	v_pk_mul_f32 v[20:21], v[20:21], v[64:65] op_sel_hi:[1,0]
	v_pk_mul_f32 v[18:19], v[18:19], v[64:65] op_sel_hi:[1,0]
	v_pk_mul_f32 v[16:17], v[16:17], v[64:65] op_sel_hi:[1,0]
	v_pk_mul_f32 v[14:15], v[14:15], v[64:65] op_sel_hi:[1,0]
	v_pk_mul_f32 v[12:13], v[12:13], v[64:65] op_sel_hi:[1,0]
	v_pk_mul_f32 v[10:11], v[10:11], v[64:65] op_sel_hi:[1,0]
	v_pk_mul_f32 v[8:9], v[8:9], v[64:65] op_sel_hi:[1,0]
	v_pk_mul_f32 v[6:7], v[6:7], v[64:65] op_sel_hi:[1,0]
	v_pk_mul_f32 v[4:5], v[4:5], v[64:65] op_sel_hi:[1,0]
	v_pk_mul_f32 v[2:3], v[2:3], v[64:65] op_sel_hi:[1,0]
	v_pk_mul_f32 v[0:1], v[0:1], v[64:65] op_sel_hi:[1,0]
	v_add_f32_e32 v65, v65, v80
	v_add_f32_e32 v65, v83, v65
	v_add_f32_e32 v65, v116, v65
	v_add_f32_e32 v65, v117, v65
	v_add_f32_e32 v65, v118, v65
	v_add_f32_e32 v65, v119, v65
	v_add_f32_e32 v65, v120, v65
	v_add_f32_e32 v65, v121, v65
	v_add_f32_e32 v65, v122, v65
	v_add_f32_e32 v65, v74, v65
	v_add_f32_e32 v65, v75, v65
	v_add_f32_e32 v65, v76, v65
	v_add_f32_e32 v65, v77, v65
	v_add_f32_e32 v65, v78, v65
	v_add_f32_e32 v65, v79, v65
	v_fmac_f32_e32 v65, v207, v64
	v_mbcnt_lo_u32_b32 v64, -1, 0
	v_mbcnt_hi_u32_b32 v64, -1, v64
	v_bfe_u32 v123, v76, 16, 1
	v_lshlrev_b32_e32 v64, 2, v64
	v_xor_b32_e32 v64, 0x80, v64
	ds_bpermute_b32 v64, v64, v65
	v_bfe_u32 v71, v77, 16, 1
	v_add3_u32 v123, v76, v123, s25
	v_mfma_f32_32x32x16_bf16 v[32:47], v[104:107], v[66:69], v[32:47]
	v_add3_u32 v71, v77, v71, s25
	s_waitcnt lgkmcnt(0)
	v_add_f32_e32 v64, v65, v64
	v_div_scale_f32 v65, s[2:3], v64, v64, 1.0
	v_lshrrev_b32_e32 v72, 16, v123
	v_and_or_b32 v72, v71, s10, v72
	v_and_or_b32 v71, v81, s10, v112
	v_mfma_f32_32x32x16_bf16 v[16:31], v[96:99], v[66:69], v[16:31]
	v_mfma_f32_32x32x16_bf16 v[0:15], v[88:91], v[66:69], v[0:15]
	v_rcp_f32_e32 v66, v65
	s_nop 0
	v_fma_f32 v67, -v65, v66, 1.0
	v_fmac_f32_e32 v66, v67, v66
	v_div_scale_f32 v67, vcc, 1.0, v64, 1.0
	v_mfma_f32_32x32x16_bf16 v[48:63], v[108:111], v[70:73], v[48:63]
	v_mul_f32_e32 v68, v67, v66
	v_fma_f32 v69, -v65, v68, v67
	v_fmac_f32_e32 v68, v69, v66
	v_fma_f32 v65, -v65, v68, v67
	v_div_fmas_f32 v65, v65, v66, v68
	v_div_fixup_f32 v66, v65, v64, 1.0
	v_lshl_add_u64 v[64:65], s[0:1], 0, v[200:201]
	s_nop 4
	v_mov_b32_e32 v68, v48
	v_mov_b32_e32 v69, v50
	v_pk_mul_f32 v[68:69], v[68:69], v[66:67] op_sel_hi:[1,0]
	v_mov_b32_e32 v50, v49
	v_pk_mul_f32 v[48:49], v[50:51], v[66:67] op_sel_hi:[1,0]
	v_and_b32_sdwa v51, v68, v231 dst_sel:DWORD dst_unused:UNUSED_PAD src0_sel:WORD_1 src1_sel:DWORD
	v_add3_u32 v51, v68, v51, s25
	v_and_b32_sdwa v67, v49, v231 dst_sel:DWORD dst_unused:UNUSED_PAD src0_sel:WORD_1 src1_sel:DWORD
	v_and_b32_sdwa v68, v48, v231 dst_sel:DWORD dst_unused:UNUSED_PAD src0_sel:WORD_1 src1_sel:DWORD
	v_and_b32_sdwa v50, v69, v231 dst_sel:DWORD dst_unused:UNUSED_PAD src0_sel:WORD_1 src1_sel:DWORD
	v_add3_u32 v49, v49, v67, s25
	v_add3_u32 v48, v48, v68, s25
	v_add3_u32 v50, v69, v50, s25
	v_and_b32_e32 v49, 0xffff0000, v49
	v_and_b32_e32 v48, 0xffff0000, v48
	v_lshl_add_u64 v[64:65], v[64:65], 0, v[202:203]
	v_or_b32_sdwa v49, v49, v50 dst_sel:DWORD dst_unused:UNUSED_PAD src0_sel:DWORD src1_sel:WORD_1
	v_or_b32_sdwa v48, v48, v51 dst_sel:DWORD dst_unused:UNUSED_PAD src0_sel:DWORD src1_sel:WORD_1
	global_store_dwordx2 v[64:65], v[48:49], off
	v_mov_b32_e32 v48, v52
	v_mov_b32_e32 v49, v54
	v_pk_mul_f32 v[48:49], v[48:49], v[66:67] op_sel_hi:[1,0]
	v_mov_b32_e32 v54, v53
	v_pk_mul_f32 v[50:51], v[54:55], v[66:67] op_sel_hi:[1,0]
	v_and_b32_sdwa v52, v49, v231 dst_sel:DWORD dst_unused:UNUSED_PAD src0_sel:WORD_1 src1_sel:DWORD
	v_and_b32_sdwa v53, v48, v231 dst_sel:DWORD dst_unused:UNUSED_PAD src0_sel:WORD_1 src1_sel:DWORD
	v_add3_u32 v48, v48, v53, s25
	v_add3_u32 v49, v49, v52, s25
	v_and_b32_sdwa v52, v51, v231 dst_sel:DWORD dst_unused:UNUSED_PAD src0_sel:WORD_1 src1_sel:DWORD
	v_and_b32_sdwa v53, v50, v231 dst_sel:DWORD dst_unused:UNUSED_PAD src0_sel:WORD_1 src1_sel:DWORD
	v_add3_u32 v51, v51, v52, s25
	v_add3_u32 v50, v50, v53, s25
	v_and_b32_e32 v51, 0xffff0000, v51
	v_and_b32_e32 v50, 0xffff0000, v50
	v_or_b32_sdwa v49, v51, v49 dst_sel:DWORD dst_unused:UNUSED_PAD src0_sel:DWORD src1_sel:WORD_1
	v_or_b32_sdwa v48, v50, v48 dst_sel:DWORD dst_unused:UNUSED_PAD src0_sel:DWORD src1_sel:WORD_1
	global_store_dwordx2 v[64:65], v[48:49], off offset:16
	v_mov_b32_e32 v48, v56
	v_mov_b32_e32 v49, v58
	v_pk_mul_f32 v[48:49], v[48:49], v[66:67] op_sel_hi:[1,0]
	v_mov_b32_e32 v58, v57
	v_pk_mul_f32 v[50:51], v[58:59], v[66:67] op_sel_hi:[1,0]
	v_and_b32_sdwa v52, v49, v231 dst_sel:DWORD dst_unused:UNUSED_PAD src0_sel:WORD_1 src1_sel:DWORD
	v_and_b32_sdwa v53, v48, v231 dst_sel:DWORD dst_unused:UNUSED_PAD src0_sel:WORD_1 src1_sel:DWORD
	v_add3_u32 v48, v48, v53, s25
	v_add3_u32 v49, v49, v52, s25
	v_and_b32_sdwa v52, v51, v231 dst_sel:DWORD dst_unused:UNUSED_PAD src0_sel:WORD_1 src1_sel:DWORD
	v_and_b32_sdwa v53, v50, v231 dst_sel:DWORD dst_unused:UNUSED_PAD src0_sel:WORD_1 src1_sel:DWORD
	v_add3_u32 v51, v51, v52, s25
	v_add3_u32 v50, v50, v53, s25
	v_and_b32_e32 v51, 0xffff0000, v51
	v_and_b32_e32 v50, 0xffff0000, v50
	s_waitcnt vmcnt(2)
	v_mfma_f32_32x32x16_bf16 v[32:47], v[100:103], v[70:73], v[32:47]
	v_or_b32_sdwa v49, v51, v49 dst_sel:DWORD dst_unused:UNUSED_PAD src0_sel:DWORD src1_sel:WORD_1
	v_or_b32_sdwa v48, v50, v48 dst_sel:DWORD dst_unused:UNUSED_PAD src0_sel:DWORD src1_sel:WORD_1
	global_store_dwordx2 v[64:65], v[48:49], off offset:32
	v_mov_b32_e32 v48, v60
	v_mov_b32_e32 v49, v62
	v_pk_mul_f32 v[48:49], v[48:49], v[66:67] op_sel_hi:[1,0]
	v_mov_b32_e32 v62, v61
	v_pk_mul_f32 v[50:51], v[62:63], v[66:67] op_sel_hi:[1,0]
	v_and_b32_sdwa v52, v49, v231 dst_sel:DWORD dst_unused:UNUSED_PAD src0_sel:WORD_1 src1_sel:DWORD
	v_and_b32_sdwa v53, v48, v231 dst_sel:DWORD dst_unused:UNUSED_PAD src0_sel:WORD_1 src1_sel:DWORD
	v_add3_u32 v48, v48, v53, s25
	v_add3_u32 v49, v49, v52, s25
	v_and_b32_sdwa v52, v51, v231 dst_sel:DWORD dst_unused:UNUSED_PAD src0_sel:WORD_1 src1_sel:DWORD
	v_and_b32_sdwa v53, v50, v231 dst_sel:DWORD dst_unused:UNUSED_PAD src0_sel:WORD_1 src1_sel:DWORD
	v_add3_u32 v51, v51, v52, s25
	v_add3_u32 v50, v50, v53, s25
	v_and_b32_e32 v51, 0xffff0000, v51
	v_and_b32_e32 v50, 0xffff0000, v50
	v_or_b32_sdwa v49, v51, v49 dst_sel:DWORD dst_unused:UNUSED_PAD src0_sel:DWORD src1_sel:WORD_1
	v_or_b32_sdwa v48, v50, v48 dst_sel:DWORD dst_unused:UNUSED_PAD src0_sel:DWORD src1_sel:WORD_1
	global_store_dwordx2 v[64:65], v[48:49], off offset:48
	v_mov_b32_e32 v48, v32
	v_mov_b32_e32 v49, v34
	v_pk_mul_f32 v[48:49], v[48:49], v[66:67] op_sel_hi:[1,0]
	v_mov_b32_e32 v34, v33
	v_pk_mul_f32 v[32:33], v[34:35], v[66:67] op_sel_hi:[1,0]
	v_and_b32_sdwa v34, v49, v231 dst_sel:DWORD dst_unused:UNUSED_PAD src0_sel:WORD_1 src1_sel:DWORD
	v_and_b32_sdwa v35, v48, v231 dst_sel:DWORD dst_unused:UNUSED_PAD src0_sel:WORD_1 src1_sel:DWORD
	v_add3_u32 v35, v48, v35, s25
	v_add3_u32 v34, v49, v34, s25
	v_and_b32_sdwa v48, v33, v231 dst_sel:DWORD dst_unused:UNUSED_PAD src0_sel:WORD_1 src1_sel:DWORD
	v_and_b32_sdwa v49, v32, v231 dst_sel:DWORD dst_unused:UNUSED_PAD src0_sel:WORD_1 src1_sel:DWORD
	v_add3_u32 v33, v33, v48, s25
	v_add3_u32 v32, v32, v49, s25
	v_and_b32_e32 v33, 0xffff0000, v33
	v_and_b32_e32 v32, 0xffff0000, v32
	v_or_b32_sdwa v33, v33, v34 dst_sel:DWORD dst_unused:UNUSED_PAD src0_sel:DWORD src1_sel:WORD_1
	v_or_b32_sdwa v32, v32, v35 dst_sel:DWORD dst_unused:UNUSED_PAD src0_sel:DWORD src1_sel:WORD_1
	global_store_dwordx2 v[64:65], v[32:33], off offset:64
	v_mov_b32_e32 v32, v36
	v_mov_b32_e32 v33, v38
	v_pk_mul_f32 v[32:33], v[32:33], v[66:67] op_sel_hi:[1,0]
	v_mov_b32_e32 v38, v37
	v_pk_mul_f32 v[34:35], v[38:39], v[66:67] op_sel_hi:[1,0]
	v_and_b32_sdwa v36, v33, v231 dst_sel:DWORD dst_unused:UNUSED_PAD src0_sel:WORD_1 src1_sel:DWORD
	v_and_b32_sdwa v37, v32, v231 dst_sel:DWORD dst_unused:UNUSED_PAD src0_sel:WORD_1 src1_sel:DWORD
	v_add3_u32 v32, v32, v37, s25
	v_add3_u32 v33, v33, v36, s25
	v_and_b32_sdwa v36, v35, v231 dst_sel:DWORD dst_unused:UNUSED_PAD src0_sel:WORD_1 src1_sel:DWORD
	v_and_b32_sdwa v37, v34, v231 dst_sel:DWORD dst_unused:UNUSED_PAD src0_sel:WORD_1 src1_sel:DWORD
	v_add3_u32 v35, v35, v36, s25
	v_add3_u32 v34, v34, v37, s25
	v_and_b32_e32 v35, 0xffff0000, v35
	v_and_b32_e32 v34, 0xffff0000, v34
	v_or_b32_sdwa v33, v35, v33 dst_sel:DWORD dst_unused:UNUSED_PAD src0_sel:DWORD src1_sel:WORD_1
	v_or_b32_sdwa v32, v34, v32 dst_sel:DWORD dst_unused:UNUSED_PAD src0_sel:DWORD src1_sel:WORD_1
	global_store_dwordx2 v[64:65], v[32:33], off offset:80
	v_mov_b32_e32 v32, v40
	v_mov_b32_e32 v33, v42
	v_pk_mul_f32 v[32:33], v[32:33], v[66:67] op_sel_hi:[1,0]
	v_mov_b32_e32 v42, v41
	v_pk_mul_f32 v[34:35], v[42:43], v[66:67] op_sel_hi:[1,0]
	v_and_b32_sdwa v36, v33, v231 dst_sel:DWORD dst_unused:UNUSED_PAD src0_sel:WORD_1 src1_sel:DWORD
	v_and_b32_sdwa v37, v32, v231 dst_sel:DWORD dst_unused:UNUSED_PAD src0_sel:WORD_1 src1_sel:DWORD
	v_add3_u32 v32, v32, v37, s25
	v_add3_u32 v33, v33, v36, s25
	v_and_b32_sdwa v36, v35, v231 dst_sel:DWORD dst_unused:UNUSED_PAD src0_sel:WORD_1 src1_sel:DWORD
	v_and_b32_sdwa v37, v34, v231 dst_sel:DWORD dst_unused:UNUSED_PAD src0_sel:WORD_1 src1_sel:DWORD
	v_add3_u32 v35, v35, v36, s25
	v_add3_u32 v34, v34, v37, s25
	v_and_b32_e32 v35, 0xffff0000, v35
	v_and_b32_e32 v34, 0xffff0000, v34
	v_mfma_f32_32x32x16_bf16 v[16:31], v[92:95], v[70:73], v[16:31]
	v_or_b32_sdwa v33, v35, v33 dst_sel:DWORD dst_unused:UNUSED_PAD src0_sel:DWORD src1_sel:WORD_1
	v_or_b32_sdwa v32, v34, v32 dst_sel:DWORD dst_unused:UNUSED_PAD src0_sel:DWORD src1_sel:WORD_1
	global_store_dwordx2 v[64:65], v[32:33], off offset:96
	v_mov_b32_e32 v32, v44
	v_mov_b32_e32 v33, v46
	v_pk_mul_f32 v[32:33], v[32:33], v[66:67] op_sel_hi:[1,0]
	v_mov_b32_e32 v46, v45
	v_pk_mul_f32 v[34:35], v[46:47], v[66:67] op_sel_hi:[1,0]
	v_and_b32_sdwa v36, v33, v231 dst_sel:DWORD dst_unused:UNUSED_PAD src0_sel:WORD_1 src1_sel:DWORD
	v_and_b32_sdwa v37, v32, v231 dst_sel:DWORD dst_unused:UNUSED_PAD src0_sel:WORD_1 src1_sel:DWORD
	v_add3_u32 v32, v32, v37, s25
	v_add3_u32 v33, v33, v36, s25
	v_and_b32_sdwa v36, v35, v231 dst_sel:DWORD dst_unused:UNUSED_PAD src0_sel:WORD_1 src1_sel:DWORD
	v_and_b32_sdwa v37, v34, v231 dst_sel:DWORD dst_unused:UNUSED_PAD src0_sel:WORD_1 src1_sel:DWORD
	v_add3_u32 v35, v35, v36, s25
	v_add3_u32 v34, v34, v37, s25
	v_and_b32_e32 v35, 0xffff0000, v35
	v_and_b32_e32 v34, 0xffff0000, v34
	v_or_b32_sdwa v33, v35, v33 dst_sel:DWORD dst_unused:UNUSED_PAD src0_sel:DWORD src1_sel:WORD_1
	v_or_b32_sdwa v32, v34, v32 dst_sel:DWORD dst_unused:UNUSED_PAD src0_sel:DWORD src1_sel:WORD_1
	global_store_dwordx2 v[64:65], v[32:33], off offset:112
	v_mov_b32_e32 v32, v16
	v_mov_b32_e32 v33, v18
	v_pk_mul_f32 v[32:33], v[32:33], v[66:67] op_sel_hi:[1,0]
	v_mov_b32_e32 v18, v17
	v_pk_mul_f32 v[16:17], v[18:19], v[66:67] op_sel_hi:[1,0]
	v_and_b32_sdwa v18, v33, v231 dst_sel:DWORD dst_unused:UNUSED_PAD src0_sel:WORD_1 src1_sel:DWORD
	v_and_b32_sdwa v19, v32, v231 dst_sel:DWORD dst_unused:UNUSED_PAD src0_sel:WORD_1 src1_sel:DWORD
	v_add3_u32 v19, v32, v19, s25
	v_add3_u32 v18, v33, v18, s25
	v_and_b32_sdwa v32, v17, v231 dst_sel:DWORD dst_unused:UNUSED_PAD src0_sel:WORD_1 src1_sel:DWORD
	v_and_b32_sdwa v33, v16, v231 dst_sel:DWORD dst_unused:UNUSED_PAD src0_sel:WORD_1 src1_sel:DWORD
	v_add3_u32 v17, v17, v32, s25
	v_add3_u32 v16, v16, v33, s25
	v_and_b32_e32 v17, 0xffff0000, v17
	v_and_b32_e32 v16, 0xffff0000, v16
	v_or_b32_sdwa v17, v17, v18 dst_sel:DWORD dst_unused:UNUSED_PAD src0_sel:DWORD src1_sel:WORD_1
	v_or_b32_sdwa v16, v16, v19 dst_sel:DWORD dst_unused:UNUSED_PAD src0_sel:DWORD src1_sel:WORD_1
	global_store_dwordx2 v[64:65], v[16:17], off offset:128
	v_mov_b32_e32 v16, v20
	v_mov_b32_e32 v17, v22
	v_pk_mul_f32 v[16:17], v[16:17], v[66:67] op_sel_hi:[1,0]
	v_mov_b32_e32 v22, v21
	v_pk_mul_f32 v[18:19], v[22:23], v[66:67] op_sel_hi:[1,0]
	v_and_b32_sdwa v20, v17, v231 dst_sel:DWORD dst_unused:UNUSED_PAD src0_sel:WORD_1 src1_sel:DWORD
	v_and_b32_sdwa v21, v16, v231 dst_sel:DWORD dst_unused:UNUSED_PAD src0_sel:WORD_1 src1_sel:DWORD
	v_add3_u32 v16, v16, v21, s25
	v_add3_u32 v17, v17, v20, s25
	v_and_b32_sdwa v20, v19, v231 dst_sel:DWORD dst_unused:UNUSED_PAD src0_sel:WORD_1 src1_sel:DWORD
	v_and_b32_sdwa v21, v18, v231 dst_sel:DWORD dst_unused:UNUSED_PAD src0_sel:WORD_1 src1_sel:DWORD
	v_add3_u32 v19, v19, v20, s25
	v_add3_u32 v18, v18, v21, s25
	v_and_b32_e32 v19, 0xffff0000, v19
	v_and_b32_e32 v18, 0xffff0000, v18
	v_or_b32_sdwa v17, v19, v17 dst_sel:DWORD dst_unused:UNUSED_PAD src0_sel:DWORD src1_sel:WORD_1
	v_or_b32_sdwa v16, v18, v16 dst_sel:DWORD dst_unused:UNUSED_PAD src0_sel:DWORD src1_sel:WORD_1
	global_store_dwordx2 v[64:65], v[16:17], off offset:144
	v_mov_b32_e32 v16, v24
	v_mov_b32_e32 v17, v26
	v_pk_mul_f32 v[16:17], v[16:17], v[66:67] op_sel_hi:[1,0]
	v_mov_b32_e32 v26, v25
	v_pk_mul_f32 v[18:19], v[26:27], v[66:67] op_sel_hi:[1,0]
	v_and_b32_sdwa v20, v17, v231 dst_sel:DWORD dst_unused:UNUSED_PAD src0_sel:WORD_1 src1_sel:DWORD
	v_and_b32_sdwa v21, v16, v231 dst_sel:DWORD dst_unused:UNUSED_PAD src0_sel:WORD_1 src1_sel:DWORD
	v_add3_u32 v16, v16, v21, s25
	v_add3_u32 v17, v17, v20, s25
	v_and_b32_sdwa v20, v19, v231 dst_sel:DWORD dst_unused:UNUSED_PAD src0_sel:WORD_1 src1_sel:DWORD
	v_and_b32_sdwa v21, v18, v231 dst_sel:DWORD dst_unused:UNUSED_PAD src0_sel:WORD_1 src1_sel:DWORD
	v_add3_u32 v19, v19, v20, s25
	v_add3_u32 v18, v18, v21, s25
	v_and_b32_e32 v19, 0xffff0000, v19
	v_and_b32_e32 v18, 0xffff0000, v18
	v_mfma_f32_32x32x16_bf16 v[0:15], v[84:87], v[70:73], v[0:15]
	v_or_b32_sdwa v17, v19, v17 dst_sel:DWORD dst_unused:UNUSED_PAD src0_sel:DWORD src1_sel:WORD_1
	v_or_b32_sdwa v16, v18, v16 dst_sel:DWORD dst_unused:UNUSED_PAD src0_sel:DWORD src1_sel:WORD_1
	global_store_dwordx2 v[64:65], v[16:17], off offset:160
	v_mov_b32_e32 v16, v28
	v_mov_b32_e32 v17, v30
	v_pk_mul_f32 v[16:17], v[16:17], v[66:67] op_sel_hi:[1,0]
	v_mov_b32_e32 v30, v29
	v_pk_mul_f32 v[18:19], v[30:31], v[66:67] op_sel_hi:[1,0]
	v_and_b32_sdwa v20, v17, v231 dst_sel:DWORD dst_unused:UNUSED_PAD src0_sel:WORD_1 src1_sel:DWORD
	v_and_b32_sdwa v21, v16, v231 dst_sel:DWORD dst_unused:UNUSED_PAD src0_sel:WORD_1 src1_sel:DWORD
	v_add3_u32 v16, v16, v21, s25
	v_add3_u32 v17, v17, v20, s25
	v_and_b32_sdwa v20, v19, v231 dst_sel:DWORD dst_unused:UNUSED_PAD src0_sel:WORD_1 src1_sel:DWORD
	v_and_b32_sdwa v21, v18, v231 dst_sel:DWORD dst_unused:UNUSED_PAD src0_sel:WORD_1 src1_sel:DWORD
	v_add3_u32 v19, v19, v20, s25
	v_add3_u32 v18, v18, v21, s25
	v_and_b32_e32 v19, 0xffff0000, v19
	v_and_b32_e32 v18, 0xffff0000, v18
	v_or_b32_sdwa v17, v19, v17 dst_sel:DWORD dst_unused:UNUSED_PAD src0_sel:DWORD src1_sel:WORD_1
	v_or_b32_sdwa v16, v18, v16 dst_sel:DWORD dst_unused:UNUSED_PAD src0_sel:DWORD src1_sel:WORD_1
	global_store_dwordx2 v[64:65], v[16:17], off offset:176
	v_mov_b32_e32 v16, v0
	v_mov_b32_e32 v17, v2
	v_pk_mul_f32 v[16:17], v[16:17], v[66:67] op_sel_hi:[1,0]
	v_mov_b32_e32 v2, v1
	v_pk_mul_f32 v[0:1], v[2:3], v[66:67] op_sel_hi:[1,0]
	v_and_b32_sdwa v2, v17, v231 dst_sel:DWORD dst_unused:UNUSED_PAD src0_sel:WORD_1 src1_sel:DWORD
	v_and_b32_sdwa v3, v16, v231 dst_sel:DWORD dst_unused:UNUSED_PAD src0_sel:WORD_1 src1_sel:DWORD
	v_add3_u32 v3, v16, v3, s25
	v_add3_u32 v2, v17, v2, s25
	v_and_b32_sdwa v16, v1, v231 dst_sel:DWORD dst_unused:UNUSED_PAD src0_sel:WORD_1 src1_sel:DWORD
	v_and_b32_sdwa v17, v0, v231 dst_sel:DWORD dst_unused:UNUSED_PAD src0_sel:WORD_1 src1_sel:DWORD
	v_add3_u32 v1, v1, v16, s25
	v_add3_u32 v0, v0, v17, s25
	v_and_b32_e32 v1, 0xffff0000, v1
	v_and_b32_e32 v0, 0xffff0000, v0
	v_or_b32_sdwa v1, v1, v2 dst_sel:DWORD dst_unused:UNUSED_PAD src0_sel:DWORD src1_sel:WORD_1
	v_or_b32_sdwa v0, v0, v3 dst_sel:DWORD dst_unused:UNUSED_PAD src0_sel:DWORD src1_sel:WORD_1
	global_store_dwordx2 v[64:65], v[0:1], off offset:192
	v_mov_b32_e32 v0, v4
	v_mov_b32_e32 v1, v6
	v_pk_mul_f32 v[0:1], v[0:1], v[66:67] op_sel_hi:[1,0]
	v_mov_b32_e32 v6, v5
	v_pk_mul_f32 v[2:3], v[6:7], v[66:67] op_sel_hi:[1,0]
	v_and_b32_sdwa v4, v1, v231 dst_sel:DWORD dst_unused:UNUSED_PAD src0_sel:WORD_1 src1_sel:DWORD
	v_and_b32_sdwa v5, v0, v231 dst_sel:DWORD dst_unused:UNUSED_PAD src0_sel:WORD_1 src1_sel:DWORD
	v_add3_u32 v0, v0, v5, s25
	v_add3_u32 v1, v1, v4, s25
	v_and_b32_sdwa v4, v3, v231 dst_sel:DWORD dst_unused:UNUSED_PAD src0_sel:WORD_1 src1_sel:DWORD
	v_and_b32_sdwa v5, v2, v231 dst_sel:DWORD dst_unused:UNUSED_PAD src0_sel:WORD_1 src1_sel:DWORD
	v_add3_u32 v3, v3, v4, s25
	v_add3_u32 v2, v2, v5, s25
	v_and_b32_e32 v3, 0xffff0000, v3
	v_and_b32_e32 v2, 0xffff0000, v2
	v_or_b32_sdwa v1, v3, v1 dst_sel:DWORD dst_unused:UNUSED_PAD src0_sel:DWORD src1_sel:WORD_1
	v_or_b32_sdwa v0, v2, v0 dst_sel:DWORD dst_unused:UNUSED_PAD src0_sel:DWORD src1_sel:WORD_1
	global_store_dwordx2 v[64:65], v[0:1], off offset:208
	v_mov_b32_e32 v0, v8
	v_mov_b32_e32 v1, v10
	v_pk_mul_f32 v[0:1], v[0:1], v[66:67] op_sel_hi:[1,0]
	v_mov_b32_e32 v10, v9
	v_pk_mul_f32 v[2:3], v[10:11], v[66:67] op_sel_hi:[1,0]
	v_and_b32_sdwa v4, v1, v231 dst_sel:DWORD dst_unused:UNUSED_PAD src0_sel:WORD_1 src1_sel:DWORD
	v_and_b32_sdwa v5, v0, v231 dst_sel:DWORD dst_unused:UNUSED_PAD src0_sel:WORD_1 src1_sel:DWORD
	v_add3_u32 v0, v0, v5, s25
	v_add3_u32 v1, v1, v4, s25
	v_and_b32_sdwa v4, v3, v231 dst_sel:DWORD dst_unused:UNUSED_PAD src0_sel:WORD_1 src1_sel:DWORD
	v_and_b32_sdwa v5, v2, v231 dst_sel:DWORD dst_unused:UNUSED_PAD src0_sel:WORD_1 src1_sel:DWORD
	v_add3_u32 v3, v3, v4, s25
	v_add3_u32 v2, v2, v5, s25
	v_and_b32_e32 v3, 0xffff0000, v3
	v_and_b32_e32 v2, 0xffff0000, v2
	v_or_b32_sdwa v1, v3, v1 dst_sel:DWORD dst_unused:UNUSED_PAD src0_sel:DWORD src1_sel:WORD_1
	v_or_b32_sdwa v0, v2, v0 dst_sel:DWORD dst_unused:UNUSED_PAD src0_sel:DWORD src1_sel:WORD_1
	global_store_dwordx2 v[64:65], v[0:1], off offset:224
	v_mov_b32_e32 v0, v12
	v_mov_b32_e32 v1, v14
	v_pk_mul_f32 v[0:1], v[0:1], v[66:67] op_sel_hi:[1,0]
	v_mov_b32_e32 v14, v13
	v_pk_mul_f32 v[2:3], v[14:15], v[66:67] op_sel_hi:[1,0]
	v_and_b32_sdwa v4, v1, v231 dst_sel:DWORD dst_unused:UNUSED_PAD src0_sel:WORD_1 src1_sel:DWORD
	v_and_b32_sdwa v5, v0, v231 dst_sel:DWORD dst_unused:UNUSED_PAD src0_sel:WORD_1 src1_sel:DWORD
	v_add3_u32 v0, v0, v5, s25
	v_add3_u32 v1, v1, v4, s25
	v_and_b32_sdwa v4, v3, v231 dst_sel:DWORD dst_unused:UNUSED_PAD src0_sel:WORD_1 src1_sel:DWORD
	v_and_b32_sdwa v5, v2, v231 dst_sel:DWORD dst_unused:UNUSED_PAD src0_sel:WORD_1 src1_sel:DWORD
	v_add3_u32 v3, v3, v4, s25
	v_add3_u32 v2, v2, v5, s25
	v_and_b32_e32 v3, 0xffff0000, v3
	v_and_b32_e32 v2, 0xffff0000, v2
	v_or_b32_sdwa v1, v3, v1 dst_sel:DWORD dst_unused:UNUSED_PAD src0_sel:DWORD src1_sel:WORD_1
	v_or_b32_sdwa v0, v2, v0 dst_sel:DWORD dst_unused:UNUSED_PAD src0_sel:DWORD src1_sel:WORD_1
	global_store_dwordx2 v[64:65], v[0:1], off offset:240
	s_cbranch_scc0 .LBB0_1292
